# speedup vs baseline: 1.0742x; 1.0182x over previous
.LBB0_8:
	s_and_b64 vcc, exec, s[4:5]
	s_cbranch_vccz .LBB0_44
	s_load_dwordx16 s[4:19], s[0:1], 0x30
	s_load_dwordx2 s[28:29], s[0:1], 0x90
	s_load_dwordx8 s[20:27], s[0:1], 0x70
	s_lshl_b32 s33, s2, 9
	s_sub_u32 s2, s2, 0x100
	v_or_b32_e32 v1, s33, v0
	v_add_u32_e32 v2, 0xfffe0000, v1
	v_lshlrev_b32_e32 v3, 6, v2
	v_lshrrev_b32_e32 v4, 5, v2
	v_and_b32_e32 v3, 0x3e00, v3
	v_and_b32_e32 v4, 0x1f8, v4
	v_and_b32_e32 v5, 0xffffc007, v2
	v_or3_b32 v20, v5, v3, v4
	v_lshlrev_b32_e32 v20, 2, v20
	v_add_u32_e32 v6, 0x18000, v2
	v_lshlrev_b32_e32 v3, 6, v6
	v_lshrrev_b32_e32 v4, 5, v6
	v_and_b32_e32 v3, 0x3e00, v3
	v_and_b32_e32 v4, 0x1f8, v4
	v_and_b32_e32 v5, 0xffffc007, v6
	v_or3_b32 v21, v5, v3, v4
	v_lshlrev_b32_e32 v21, 2, v21
	v_and_b32_e32 v7, 0xffff, v2
	v_add_u32_e32 v6, 0x30000, v7
	v_lshlrev_b32_e32 v3, 6, v6
	v_lshrrev_b32_e32 v4, 5, v6
	v_and_b32_e32 v3, 0x3e00, v3
	v_and_b32_e32 v4, 0x1f8, v4
	v_and_b32_e32 v5, 0xffffc007, v6
	v_or3_b32 v22, v5, v3, v4
	v_lshlrev_b32_e32 v22, 2, v22
	v_lshlrev_b32_e32 v3, 4, v7
	v_lshrrev_b32_e32 v4, 4, v7
	v_and_b32_e32 v3, 0x780, v3
	v_and_b32_e32 v4, 0x78, v4
	v_and_b32_e32 v5, 0xf807, v7
	v_or3_b32 v23, v5, v3, v4
	v_lshlrev_b32_e32 v23, 2, v23
	v_and_b32_e32 v6, 0x7fff, v2
	v_lshlrev_b32_e32 v3, 5, v6
	v_lshrrev_b32_e32 v4, 5, v6
	v_and_b32_e32 v3, 0x1f00, v3
	v_and_b32_e32 v4, 0xf8, v4
	v_and_b32_e32 v5, 0xe007, v6
	v_or3_b32 v24, v5, v3, v4
	v_lshlrev_b32_e32 v24, 2, v24
	v_and_b32_e32 v6, 0x3fff, v2
	v_lshrrev_b32_e32 v3, 8, v6
	v_lshrrev_b32_e32 v4, 3, v6
	v_and_b32_e32 v3, 0xf0, v3
	v_and_b32_e32 v4, 15, v4
	v_or_b32_e32 v3, v3, v4
	v_cmp_gt_u32_e64 s[30:31], 40, v3
	v_lshlrev_b32_e32 v3, 8, v3
	v_lshrrev_b32_e32 v4, 4, v6
	v_and_b32_e32 v4, 0xf8, v4
	v_and_b32_e32 v5, 7, v6
	v_or3_b32 v25, v3, v4, v5
	v_lshlrev_b32_e32 v25, 2, v25
	v_cndmask_b32_e64 v25, 0, v25, s[30:31]
	v_and_b32_e32 v26, 0xfff, v2
	v_lshlrev_b32_e32 v26, 2, v26
	v_lshlrev_b32_e32 v40, 1, v2
	v_add_u32_e32 v41, 0x30000, v40
	v_add_u32_e32 v42, 0x60000, v40
	v_lshlrev_b32_e32 v43, 2, v2
	v_mov_b32_e32 v44, 0
	s_waitcnt lgkmcnt(0)
	global_load_dword v30, v20, s[10:11]
	global_load_dword v31, v20, s[12:13]
	global_load_dword v32, v21, s[10:11]
	global_load_dword v33, v21, s[12:13]
	global_load_dword v34, v22, s[10:11]
	global_load_dword v35, v22, s[12:13]
	global_load_dword v36, v23, s[4:5]
	global_load_dword v37, v24, s[8:9]
	global_load_dword v38, v25, s[6:7]
	global_load_dword v39, v26, s[14:15]
	s_mov_b32 s6, 0x3fb8aa3b
	s_mov_b32 s7, 0xc2ce8ed0
	s_mov_b32 s8, 0x42b17218
	v_mov_b32_e32 v45, 0x7f800000
	s_waitcnt vmcnt(0)
	v_cvt_f16_f32_e32 v30, v30
	v_cvt_f16_f32_e32 v31, v31
	v_cvt_f16_f32_e32 v32, v32
	v_cvt_f16_f32_e32 v33, v33
	global_store_short v40, v30, s[22:23]
	global_store_short v40, v31, s[24:25]
	global_store_short v41, v32, s[22:23]
	global_store_short v41, v33, s[24:25]
	s_cmp_lt_u32 s2, 0x80
	s_cbranch_scc0 .LBB0_44
	v_cvt_f16_f32_e32 v34, v34
	v_cvt_f16_f32_e32 v35, v35
	v_cvt_f16_f32_e32 v36, v36
	global_store_short v42, v34, s[22:23]
	global_store_short v42, v35, s[24:25]
	global_store_short v40, v36, s[16:17]
	s_cmp_lt_u32 s2, 64
	s_cbranch_scc0 .LBB0_44
	v_cvt_f16_f32_e32 v37, v37
	global_store_short v40, v37, s[20:21]
	s_cmp_lt_u32 s2, 32
	s_cbranch_scc0 .LBB0_44
	global_store_dword v43, v44, s[28:29]
	s_cmp_lt_u32 s2, 24
	s_cbranch_scc0 .LBB0_44
	v_cvt_f16_f32_e32 v38, v38
	s_nop 0
	v_cndmask_b32_e64 v38, 0, v38, s[30:31]
	global_store_short v40, v38, s[18:19]
	s_cmp_lt_u32 s2, 8
	s_cbranch_scc0 .LBB0_44
	v_mul_f32_e32 v9, 0x3fb8aa3b, v39
	v_rndne_f32_e32 v10, v9
	v_fma_f32 v11, v39, s6, -v9
	v_sub_f32_e32 v9, v9, v10
	v_fmac_f32_e32 v11, 0x32a5705f, v39
	v_add_f32_e32 v9, v9, v11
	v_cvt_i32_f32_e32 v10, v10
	v_exp_f32_e32 v9, v9
	v_cmp_ngt_f32_e32 vcc, s7, v39
	v_ldexp_f32 v9, v9, v10
	s_nop 0
	v_cndmask_b32_e32 v9, 0, v9, vcc
	v_cmp_nlt_f32_e32 vcc, s8, v39
	s_nop 1
	v_cndmask_b32_e32 v8, v45, v9, vcc
	v_mul_f32_e32 v8, 0xbfb8aa3b, v8
	global_store_dword v43, v8, s[26:27]
